# adds LN waits moved to consumers, LN layer-0 input row prefetch, attention epilogue gain pipelining, conv waits
# speedup vs baseline: 1.0128x; 1.0128x over previous
.LBB0_513:
	s_mul_i32 s27, s9, 0xab
	s_bfe_u32 s27, s27, 0x70009
	s_mul_i32 s27, s27, 3
	s_sub_i32 s27, s9, s27
	s_and_b32 s27, s27, 0xff
	s_mul_i32 s37, s36, 3
	s_add_i32 s27, s27, s37
	s_cmp_lt_u32 s9, 6
	s_mul_hi_u32 s37, s27, 0xc000
	s_mul_i32 s27, s27, 0xc000
	s_cselect_b32 s40, 0x2000, s77
	s_add_u32 s27, s6, s27
	s_addc_u32 s37, s8, s37
	s_cmp_gt_u32 s9, 2
	s_cselect_b32 s40, s40, 0x1800
	s_lshl_b32 s40, s40, 2
	s_add_u32 s40, s27, s40
	s_addc_u32 s41, s37, 0
	v_lshl_add_u64 v[8:9], v[4:5], 2, s[40:41]
	global_load_dwordx4 v[8:11], v[8:9], off
	s_add_i32 s9, s9, 1
	s_cmp_eq_u32 s9, 9
	s_waitcnt vmcnt(0)
	ds_write_b128 v6, v[8:11]
	v_add_u32_e32 v6, 0x2000, v6
	s_cbranch_scc0 .LBB0_513
	s_andn2_b64 vcc, exec, s[42:43]
	s_waitcnt lgkmcnt(0)
	s_barrier
	s_cbranch_vccnz .LBB0_545
	v_add_u32_e32 v145, 0, v2
	ds_read_b128 v[4:7], v145
	ds_read_b128 v[8:11], v145 offset:1024
	ds_read_b128 v[12:15], v145 offset:8192
	ds_read_b128 v[16:19], v145 offset:9216
	ds_read_b128 v[20:23], v145 offset:2048
	ds_read_b128 v[24:27], v145 offset:3072
	ds_read_b128 v[28:31], v145 offset:10240
	ds_read_b128 v[32:35], v145 offset:11264
	ds_read_b128 v[36:39], v145 offset:4096
	ds_read_b128 v[40:43], v145 offset:5120
	ds_read_b128 v[44:47], v145 offset:12288
	ds_read_b128 v[48:51], v145 offset:13312
	ds_read_b128 v[52:55], v145 offset:6144
	ds_read_b128 v[56:59], v145 offset:7168
	ds_read_b128 v[60:63], v145 offset:14336
	ds_read_b128 v[64:67], v145 offset:15360
	s_cmp_lg_u32 s36, 0
	s_cselect_b64 s[44:45], -1, 0
	s_add_u32 s27, s0, 16
	s_addc_u32 s37, s1, 0
	s_ashr_i32 s53, s52, 31
	s_lshl_b64 s[8:9], s[52:53], 2
	s_add_u32 s56, s8, 0x3d200000
	s_addc_u32 s57, s9, 0
	s_lshl_b64 s[8:9], s[52:53], 11
	v_or_b32_e32 v146, s8, v144
	v_mov_b32_e32 v147, s9
	v_lshl_or_b32 v148, v68, 2, s8
	v_mov_b32_e32 v149, s9
	s_lshl_b64 s[8:9], s[52:53], 12
	v_readlane_b32 s6, v253, 11
	v_or_b32_e32 v150, s8, v2
	s_add_i32 s8, s6, s50
	v_mov_b32_e32 v151, s9
	s_ashr_i32 s9, s8, 31
	s_lshl_b64 s[42:43], s[8:9], 12
	s_lshl_b64 s[8:9], s[8:9], 11
	v_cmp_eq_u32_e64 s[40:41], 0, v68
	s_lshl_b64 s[46:47], s[52:53], 13
	v_or_b32_e32 v152, s42, v2
	v_mov_b32_e32 v153, s43
	v_or_b32_e32 v154, s8, v144
	v_mov_b32_e32 v155, s9
	s_and_b64 vcc, exec, s[44:45]
	s_cbranch_vccnz .Lln0_pre_done
	v_lshlrev_b32_e32 v228, 2, v144
	s_add_i32 s6, s52, 0xffffc000
	s_lshl_b64 s[42:43], s[6:7], 13
	s_cmpk_lt_i32 s52, 0x4000
	s_cselect_b32 s9, s1, s37
	s_cselect_b32 s8, s0, s27
	s_cselect_b32 s100, s46, s42
	s_cselect_b32 s101, s47, s43
	s_load_dwordx2 s[8:9], s[8:9], 0x0
	s_waitcnt lgkmcnt(0)
	s_add_u32 s8, s8, s100
	s_addc_u32 s9, s9, s101
	global_load_dwordx4 v[182:185], v228, s[8:9] offset:16
	global_load_dwordx4 v[186:189], v228, s[8:9]
	global_load_dwordx4 v[190:193], v228, s[8:9] offset:2064
	global_load_dwordx4 v[194:197], v228, s[8:9] offset:2048
	s_add_u32 s8, s8, 0x1000
	s_addc_u32 s9, s9, 0
	global_load_dwordx4 v[198:201], v228, s[8:9]
	global_load_dwordx4 v[202:205], v228, s[8:9] offset:16
	global_load_dwordx4 v[220:223], v228, s[8:9] offset:2048
	global_load_dwordx4 v[224:227], v228, s[8:9] offset:2064
.Lln0_pre_done:
	s_waitcnt vmcnt(0)
	s_branch .LBB0_517
.LBB0_516:
	s_or_b64 exec, exec, s[8:9]
	s_waitcnt vmcnt(16)
	s_add_u32 s56, s56, s12
	s_addc_u32 s57, s57, s13
	s_add_u32 s46, s46, s18
	v_mov_b64_e32 v[86:87], v[70:71]
	v_mov_b64_e32 v[90:91], v[74:75]
	v_mov_b64_e32 v[94:95], v[78:79]
	v_mov_b64_e32 v[98:99], v[82:83]
	v_lshl_add_u64 v[146:147], v[146:147], 0, s[14:15]
	v_lshl_add_u64 v[148:149], v[148:149], 0, s[14:15]
	v_lshl_add_u64 v[150:151], v[150:151], 0, s[16:17]
	s_addc_u32 s47, s47, s19
	v_lshl_add_u64 v[152:153], v[152:153], 0, s[16:17]
	v_lshl_add_u64 v[154:155], v[154:155], 0, s[14:15]
	s_andn2_b64 vcc, exec, s[50:51]
	v_mov_b64_e32 v[84:85], v[68:69]
	v_mov_b64_e32 v[88:89], v[72:73]
	v_mov_b64_e32 v[92:93], v[76:77]
	v_mov_b64_e32 v[96:97], v[80:81]
	v_mov_b64_e32 v[164:165], v[162:163]
	v_mov_b64_e32 v[166:167], v[160:161]
	v_mov_b64_e32 v[168:169], v[158:159]
	v_mov_b64_e32 v[170:171], v[156:157]
	s_mov_b32 s52, s53
	s_cbranch_vccz .LBB0_545

.LBB0_529:
	s_add_i32 s6, s52, 0xffffc000
	s_lshl_b64 s[42:43], s[6:7], 13
	s_andn2_b64 vcc, exec, s[8:9]
	v_lshlrev_b32_e32 v2, 2, v144
	s_cbranch_vccnz .LBB0_531
	s_waitcnt vmcnt(17)
	s_nop 0
	v_mov_b32_e32 v96, v182
	v_mov_b32_e32 v97, v183
	v_mov_b32_e32 v98, v184
	v_mov_b32_e32 v99, v185
	v_mov_b32_e32 v100, v186
	v_mov_b32_e32 v101, v187
	v_mov_b32_e32 v102, v188
	v_mov_b32_e32 v103, v189

.LBB0_533:
	v_mov_b32_e32 v92, v190
	v_mov_b32_e32 v93, v191
	v_mov_b32_e32 v94, v192
	v_mov_b32_e32 v95, v193
	v_mov_b32_e32 v108, v194
	v_mov_b32_e32 v109, v195
	v_mov_b32_e32 v110, v196
	v_mov_b32_e32 v111, v197

.LBB0_536:
	v_mov_b32_e32 v120, v198
	v_mov_b32_e32 v121, v199
	v_mov_b32_e32 v122, v200
	v_mov_b32_e32 v123, v201
	v_mov_b32_e32 v88, v202
	v_mov_b32_e32 v89, v203
	v_mov_b32_e32 v90, v204
	v_mov_b32_e32 v91, v205

.LBB0_539:
	v_mov_b32_e32 v128, v220
	v_mov_b32_e32 v129, v221
	v_mov_b32_e32 v130, v222
	v_mov_b32_e32 v131, v223
	v_mov_b32_e32 v140, v224
	v_mov_b32_e32 v141, v225
	v_mov_b32_e32 v142, v226
	v_mov_b32_e32 v143, v227
	s_and_b64 vcc, exec, s[50:51]
	s_cbranch_vccnz .Lln0_nonext
	s_add_u32 s100, s46, s18
	s_addc_u32 s101, s47, s19
	s_add_i32 s6, s53, 0xffffc000
	s_lshl_b64 s[42:43], s[6:7], 13
	s_cmpk_lt_i32 s53, 0x4000
	s_cselect_b32 s9, s1, s37
	s_cselect_b32 s8, s0, s27
	s_cselect_b32 s100, s100, s42
	s_cselect_b32 s101, s101, s43
	s_load_dwordx2 s[8:9], s[8:9], 0x0
	s_waitcnt lgkmcnt(0)
	s_add_u32 s8, s8, s100
	s_addc_u32 s9, s9, s101
	global_load_dwordx4 v[182:185], v2, s[8:9] offset:16
	global_load_dwordx4 v[186:189], v2, s[8:9]
	global_load_dwordx4 v[190:193], v2, s[8:9] offset:2064
	global_load_dwordx4 v[194:197], v2, s[8:9] offset:2048
	s_add_u32 s8, s8, 0x1000
	s_addc_u32 s9, s9, 0
	global_load_dwordx4 v[198:201], v2, s[8:9]
	global_load_dwordx4 v[202:205], v2, s[8:9] offset:16
	global_load_dwordx4 v[220:223], v2, s[8:9] offset:2048
	global_load_dwordx4 v[224:227], v2, s[8:9] offset:2064
.Lln0_nonext:
.LBB0_540:
	v_cvt_pk_f32_fp8_e32 v[84:85], v170
	v_cvt_pk_f32_fp8_sdwa v[86:87], v170 src0_sel:WORD_1
	v_cvt_pk_f32_fp8_e32 v[174:175], v171
	v_cvt_pk_f32_fp8_sdwa v[170:171], v171 src0_sel:WORD_1
	s_waitcnt lgkmcnt(5)
	v_pk_mul_f32 v[84:85], v[84:85], v[112:113]
	v_pk_fma_f32 v[100:101], v[100:101], s[34:35], v[84:85] op_sel_hi:[1,0,1]
	v_pk_mul_f32 v[84:85], v[86:87], v[114:115]
	v_add_f32_e32 v2, 0, v100
	v_pk_fma_f32 v[102:103], v[102:103], s[34:35], v[84:85] op_sel_hi:[1,0,1]
	s_waitcnt lgkmcnt(4)
	v_pk_mul_f32 v[84:85], v[174:175], v[104:105]
	v_add_f32_e32 v2, v101, v2
	v_pk_fma_f32 v[96:97], v[96:97], s[34:35], v[84:85] op_sel_hi:[1,0,1]
	v_pk_mul_f32 v[84:85], v[170:171], v[106:107]
	v_add_f32_e32 v2, v102, v2
	v_pk_fma_f32 v[98:99], v[98:99], s[34:35], v[84:85] op_sel_hi:[1,0,1]
	v_cvt_pk_f32_fp8_e32 v[84:85], v168
	v_cvt_pk_f32_fp8_sdwa v[86:87], v168 src0_sel:WORD_1
	v_add_f32_e32 v2, v103, v2
	v_cvt_pk_f32_fp8_e32 v[104:105], v169
	v_add_f32_e32 v2, v96, v2
	v_cvt_pk_f32_fp8_sdwa v[106:107], v169 src0_sel:WORD_1
	v_add_f32_e32 v2, v97, v2
	s_waitcnt lgkmcnt(3)
	v_pk_mul_f32 v[84:85], v[84:85], v[124:125]
	v_add_f32_e32 v2, v98, v2
	v_pk_fma_f32 v[108:109], v[108:109], s[34:35], v[84:85] op_sel_hi:[1,0,1]
	v_pk_mul_f32 v[84:85], v[86:87], v[126:127]
	v_add_f32_e32 v2, v99, v2
	v_pk_fma_f32 v[110:111], v[110:111], s[34:35], v[84:85] op_sel_hi:[1,0,1]
	s_waitcnt lgkmcnt(2)
	v_pk_mul_f32 v[84:85], v[104:105], v[116:117]
	v_add_f32_e32 v2, v2, v108
	v_pk_fma_f32 v[92:93], v[92:93], s[34:35], v[84:85] op_sel_hi:[1,0,1]
	v_pk_mul_f32 v[84:85], v[106:107], v[118:119]
	v_add_f32_e32 v2, v109, v2
	v_pk_fma_f32 v[94:95], v[94:95], s[34:35], v[84:85] op_sel_hi:[1,0,1]
	v_cvt_pk_f32_fp8_e32 v[84:85], v166
	v_add_f32_e32 v2, v110, v2
	v_cvt_pk_f32_fp8_sdwa v[86:87], v166 src0_sel:WORD_1
	v_add_f32_e32 v2, v111, v2
	v_cvt_pk_f32_fp8_e32 v[104:105], v167
	v_add_f32_e32 v2, v92, v2
	v_cvt_pk_f32_fp8_sdwa v[106:107], v167 src0_sel:WORD_1
	v_add_f32_e32 v2, v93, v2
	s_waitcnt lgkmcnt(1)
	v_pk_mul_f32 v[84:85], v[84:85], v[136:137]
	v_add_f32_e32 v2, v94, v2
	v_pk_fma_f32 v[112:113], v[120:121], s[34:35], v[84:85] op_sel_hi:[1,0,1]
	v_pk_mul_f32 v[84:85], v[86:87], v[138:139]
	v_add_f32_e32 v2, v95, v2
	v_pk_fma_f32 v[114:115], v[122:123], s[34:35], v[84:85] op_sel_hi:[1,0,1]
	s_waitcnt lgkmcnt(0)
	v_pk_mul_f32 v[84:85], v[104:105], v[132:133]
	v_add_f32_e32 v2, v2, v112
	v_pk_fma_f32 v[104:105], v[88:89], s[34:35], v[84:85] op_sel_hi:[1,0,1]
	v_pk_mul_f32 v[84:85], v[106:107], v[134:135]
	v_add_f32_e32 v2, v113, v2
	v_pk_fma_f32 v[106:107], v[90:91], s[34:35], v[84:85] op_sel_hi:[1,0,1]
	v_add_u32_e32 v84, 0x11800, v172
	v_add_u32_e32 v88, 0x11c00, v172
	v_add_f32_e32 v2, v114, v2
	ds_read_b128 v[84:87], v84
	ds_read_b128 v[88:91], v88
	v_cvt_pk_f32_fp8_e32 v[118:119], v164
	v_add_f32_e32 v2, v115, v2
	v_add_f32_e32 v2, v104, v2
	v_cvt_pk_f32_fp8_sdwa v[122:123], v164 src0_sel:WORD_1
	v_add_f32_e32 v2, v105, v2
	v_add_f32_e32 v2, v106, v2
	v_cvt_pk_f32_fp8_e32 v[120:121], v165
	s_waitcnt lgkmcnt(1)
	v_pk_mul_f32 v[84:85], v[118:119], v[84:85]
	v_add_f32_e32 v2, v107, v2
	v_pk_fma_f32 v[84:85], v[128:129], s[34:35], v[84:85] op_sel_hi:[1,0,1]
	v_cvt_pk_f32_fp8_sdwa v[116:117], v165 src0_sel:WORD_1
	v_pk_mul_f32 v[86:87], v[122:123], v[86:87]
	v_add_f32_e32 v2, v2, v84
	v_pk_fma_f32 v[86:87], v[130:131], s[34:35], v[86:87] op_sel_hi:[1,0,1]
	v_add_f32_e32 v2, v85, v2
	s_waitcnt lgkmcnt(0)
	v_pk_mul_f32 v[88:89], v[120:121], v[88:89]
	v_add_f32_e32 v2, v86, v2
	v_pk_fma_f32 v[88:89], v[140:141], s[34:35], v[88:89] op_sel_hi:[1,0,1]
	v_add_f32_e32 v2, v87, v2
	v_pk_mul_f32 v[90:91], v[116:117], v[90:91]
	v_add_f32_e32 v2, v88, v2
	v_pk_fma_f32 v[90:91], v[142:143], s[34:35], v[90:91] op_sel_hi:[1,0,1]
	v_add_f32_e32 v2, v89, v2
	v_add_f32_e32 v2, v90, v2
	v_add_f32_e32 v2, v91, v2
	s_nop 1
	v_add_f32_dpp v2, v2, v2 quad_perm:[1,0,3,2] row_mask:0xf bank_mask:0xf bound_ctrl:1
	s_nop 1
	v_add_f32_dpp v2, v2, v2 quad_perm:[2,3,0,1] row_mask:0xf bank_mask:0xf bound_ctrl:1
	s_nop 1
	v_add_f32_dpp v2, v2, v2 row_ror:4 row_mask:0xf bank_mask:0xf bound_ctrl:1
	s_nop 1
	v_add_f32_dpp v2, v2, v2 row_ror:8 row_mask:0xf bank_mask:0xf bound_ctrl:1
	s_nop 0
	v_readlane_b32 s6, v2, 16
	v_readlane_b32 s42, v2, 48
	v_readlane_b32 s8, v2, 0
	v_readlane_b32 s9, v2, 32
	v_mov_b32_e32 v116, s6
	v_mov_b32_e32 v117, s42
	v_pk_add_f32 v[116:117], s[8:9], v[116:117]
	s_nop 0
	v_add_f32_e32 v2, v116, v117
	v_mul_f32_e32 v2, 0x3a000000, v2
	v_pk_add_f32 v[100:101], v[100:101], v[2:3] op_sel_hi:[1,0] neg_lo:[0,1] neg_hi:[0,1]
	v_pk_add_f32 v[102:103], v[102:103], v[2:3] op_sel_hi:[1,0] neg_lo:[0,1] neg_hi:[0,1]
	v_pk_mul_f32 v[130:131], v[100:101], v[100:101]
	v_pk_add_f32 v[116:117], v[84:85], v[2:3] op_sel_hi:[1,0] neg_lo:[0,1] neg_hi:[0,1]
	v_pk_add_f32 v[118:119], v[86:87], v[2:3] op_sel_hi:[1,0] neg_lo:[0,1] neg_hi:[0,1]
	v_pk_add_f32 v[126:127], v[88:89], v[2:3] op_sel_hi:[1,0] neg_lo:[0,1] neg_hi:[0,1]
	v_pk_add_f32 v[128:129], v[90:91], v[2:3] op_sel_hi:[1,0] neg_lo:[0,1] neg_hi:[0,1]
	v_pk_add_f32 v[98:99], v[98:99], v[2:3] op_sel_hi:[1,0] neg_lo:[0,1] neg_hi:[0,1]
	v_pk_add_f32 v[96:97], v[96:97], v[2:3] op_sel_hi:[1,0] neg_lo:[0,1] neg_hi:[0,1]
	v_pk_mul_f32 v[124:125], v[102:103], v[102:103]
	v_pk_add_f32 v[132:133], v[94:95], v[2:3] op_sel_hi:[1,0] neg_lo:[0,1] neg_hi:[0,1]
	v_pk_add_f32 v[92:93], v[92:93], v[2:3] op_sel_hi:[1,0] neg_lo:[0,1] neg_hi:[0,1]
	v_pk_add_f32 v[110:111], v[110:111], v[2:3] op_sel_hi:[1,0] neg_lo:[0,1] neg_hi:[0,1]
	v_pk_add_f32 v[108:109], v[108:109], v[2:3] op_sel_hi:[1,0] neg_lo:[0,1] neg_hi:[0,1]
	v_pk_add_f32 v[106:107], v[106:107], v[2:3] op_sel_hi:[1,0] neg_lo:[0,1] neg_hi:[0,1]
	v_pk_add_f32 v[142:143], v[104:105], v[2:3] op_sel_hi:[1,0] neg_lo:[0,1] neg_hi:[0,1]
	v_pk_add_f32 v[114:115], v[114:115], v[2:3] op_sel_hi:[1,0] neg_lo:[0,1] neg_hi:[0,1]
	v_pk_add_f32 v[166:167], v[112:113], v[2:3] op_sel_hi:[1,0] neg_lo:[0,1] neg_hi:[0,1]
	v_add_f32_e32 v2, v130, v131
	v_add_f32_e32 v2, v124, v2
	v_pk_mul_f32 v[122:123], v[96:97], v[96:97]
	v_add_f32_e32 v2, v125, v2
	v_add_f32_e32 v2, v122, v2
	v_pk_mul_f32 v[120:121], v[98:99], v[98:99]
	v_add_f32_e32 v2, v123, v2
	v_add_f32_e32 v2, v120, v2
	v_pk_mul_f32 v[138:139], v[108:109], v[108:109]
	v_add_f32_e32 v2, v121, v2
	v_add_f32_e32 v2, v138, v2
	v_pk_mul_f32 v[136:137], v[110:111], v[110:111]
	v_add_f32_e32 v2, v139, v2
	v_add_f32_e32 v2, v136, v2
	v_pk_mul_f32 v[134:135], v[92:93], v[92:93]
	v_add_f32_e32 v2, v137, v2
	v_add_f32_e32 v2, v134, v2
	v_pk_mul_f32 v[94:95], v[132:133], v[132:133]
	v_add_f32_e32 v2, v135, v2
	v_add_f32_e32 v2, v94, v2
	v_pk_mul_f32 v[112:113], v[166:167], v[166:167]
	v_add_f32_e32 v2, v95, v2
	v_add_f32_e32 v2, v112, v2
	v_pk_mul_f32 v[164:165], v[114:115], v[114:115]
	v_add_f32_e32 v2, v113, v2
	v_add_f32_e32 v2, v164, v2
	v_pk_mul_f32 v[104:105], v[142:143], v[142:143]
	v_add_f32_e32 v2, v165, v2
	v_add_f32_e32 v2, v104, v2
	v_pk_mul_f32 v[140:141], v[106:107], v[106:107]
	v_add_f32_e32 v2, v105, v2
	v_add_f32_e32 v2, v140, v2
	v_pk_mul_f32 v[84:85], v[116:117], v[116:117]
	v_add_f32_e32 v2, v141, v2
	v_add_f32_e32 v2, v84, v2
	v_pk_mul_f32 v[86:87], v[118:119], v[118:119]
	v_add_f32_e32 v2, v85, v2
	v_add_f32_e32 v2, v86, v2
	v_pk_mul_f32 v[88:89], v[126:127], v[126:127]
	v_add_f32_e32 v2, v87, v2
	v_add_f32_e32 v2, v88, v2
	v_pk_mul_f32 v[90:91], v[128:129], v[128:129]
	v_add_f32_e32 v2, v89, v2
	v_add_f32_e32 v2, v90, v2
	v_add_f32_e32 v2, v91, v2
	v_lshl_add_u64 v[88:89], s[4:5], 0, v[150:151]
	s_nop 0
	v_add_f32_dpp v2, v2, v2 quad_perm:[1,0,3,2] row_mask:0xf bank_mask:0xf bound_ctrl:1
	s_nop 1
	v_add_f32_dpp v2, v2, v2 quad_perm:[2,3,0,1] row_mask:0xf bank_mask:0xf bound_ctrl:1
	s_nop 1
	v_add_f32_dpp v2, v2, v2 row_ror:4 row_mask:0xf bank_mask:0xf bound_ctrl:1
	s_nop 1
	v_add_f32_dpp v2, v2, v2 row_ror:8 row_mask:0xf bank_mask:0xf bound_ctrl:1
	s_nop 0
	v_readlane_b32 s6, v2, 16
	v_readlane_b32 s42, v2, 48
	v_readlane_b32 s8, v2, 0
	v_readlane_b32 s9, v2, 32
	v_mov_b32_e32 v84, s6
	v_mov_b32_e32 v85, s42
	v_pk_add_f32 v[84:85], s[8:9], v[84:85]
	s_mov_b32 s6, 0xb000000
	v_add_f32_e32 v2, v84, v85
	v_fmamk_f32 v2, v2, 0x3a000000, v207
	v_mul_f32_e32 v84, 0x4f800000, v2
	v_cmp_gt_f32_e32 vcc, s10, v2
	s_nop 1
	v_cndmask_b32_e32 v2, v2, v84, vcc
	v_sqrt_f32_e32 v84, v2
	s_nop 0
	v_add_u32_e32 v85, -1, v84
	v_fma_f32 v86, -v85, v84, v2
	v_cmp_ge_f32_e64 s[42:43], 0, v86
	v_add_u32_e32 v86, 1, v84
	s_nop 0
	v_cndmask_b32_e64 v85, v84, v85, s[42:43]
	v_fma_f32 v84, -v86, v84, v2
	v_cmp_lt_f32_e64 s[42:43], 0, v84
	s_nop 1
	v_cndmask_b32_e64 v84, v85, v86, s[42:43]
	v_mul_f32_e32 v85, 0x37800000, v84
	v_cndmask_b32_e32 v84, v84, v85, vcc
	v_cmp_class_f32_e32 vcc, v2, v208
	s_nop 1
	v_cndmask_b32_e32 v2, v84, v2, vcc
	v_div_scale_f32 v84, s[8:9], v2, v2, 1.0
	v_rcp_f32_e32 v85, v84
	s_nop 0
	v_fma_f32 v86, -v84, v85, 1.0
	v_fmac_f32_e32 v85, v86, v85
	v_div_scale_f32 v86, vcc, 1.0, v2, 1.0
	v_mul_f32_e32 v87, v86, v85
	v_fma_f32 v90, -v84, v87, v86
	v_fmac_f32_e32 v87, v90, v85
	v_fma_f32 v84, -v84, v87, v86
	v_div_fmas_f32 v84, v84, v85, v87
	v_div_fixup_f32 v2, v84, v2, 1.0
	v_pk_mul_f32 v[84:85], v[100:101], v[2:3] op_sel_hi:[1,0]
	v_add_co_u32_e32 v130, vcc, s6, v88
	v_pk_fma_f32 v[122:123], v[4:5], v[84:85], v[12:13]
	s_nop 0
	v_addc_co_u32_e32 v131, vcc, 0, v89, vcc
	v_add_f32_e32 v84, 0, v122
	v_add_f32_e32 v86, v123, v84
	v_pk_mul_f32 v[84:85], v[102:103], v[2:3] op_sel_hi:[1,0]
	s_nop 0
	v_pk_fma_f32 v[120:121], v[6:7], v[84:85], v[14:15]
	s_nop 0
	v_add_f32_e32 v84, v120, v86
	v_pk_mul_f32 v[86:87], v[96:97], v[2:3] op_sel_hi:[1,0]
	v_add_f32_e32 v90, v121, v84
	v_pk_fma_f32 v[102:103], v[8:9], v[86:87], v[16:17]
	v_cvt_pk_bf16_f32 v84, v122, v123
	v_add_f32_e32 v86, v102, v90
	v_add_f32_e32 v90, v103, v86
	v_pk_mul_f32 v[86:87], v[98:99], v[2:3] op_sel_hi:[1,0]
	v_cvt_pk_bf16_f32 v85, v120, v121
	v_pk_fma_f32 v[96:97], v[10:11], v[86:87], v[18:19]
	s_nop 0
	v_add_f32_e32 v86, v96, v90
	v_add_f32_e32 v90, v97, v86
	v_cvt_pk_bf16_f32 v86, v102, v103
	v_cvt_pk_bf16_f32 v87, v96, v97
	global_store_dwordx4 v[130:131], v[84:87], off
	s_nop 1
	v_pk_mul_f32 v[84:85], v[108:109], v[2:3] op_sel_hi:[1,0]
	s_nop 0
	v_pk_fma_f32 v[112:113], v[20:21], v[84:85], v[28:29]
	s_nop 0
	v_add_f32_e32 v84, v112, v90
	v_add_f32_e32 v86, v113, v84
	v_pk_mul_f32 v[84:85], v[110:111], v[2:3] op_sel_hi:[1,0]
	v_cvt_pk_bf16_f32 v98, v112, v113
	v_pk_fma_f32 v[94:95], v[22:23], v[84:85], v[30:31]
	s_nop 0
	v_add_f32_e32 v84, v94, v86
	v_add_f32_e32 v86, v95, v84
	v_pk_mul_f32 v[84:85], v[92:93], v[2:3] op_sel_hi:[1,0]
	v_cvt_pk_bf16_f32 v99, v94, v95
	v_pk_fma_f32 v[92:93], v[24:25], v[84:85], v[32:33]
	s_nop 0
	v_add_f32_e32 v84, v92, v86
	v_add_f32_e32 v86, v93, v84
	v_pk_mul_f32 v[84:85], v[132:133], v[2:3] op_sel_hi:[1,0]
	v_cvt_pk_bf16_f32 v100, v92, v93
	v_pk_fma_f32 v[90:91], v[26:27], v[84:85], v[34:35]
	s_nop 0
	v_add_f32_e32 v84, v90, v86
	v_add_f32_e32 v86, v91, v84
	v_pk_mul_f32 v[84:85], v[166:167], v[2:3] op_sel_hi:[1,0]
	v_cvt_pk_bf16_f32 v101, v90, v91
	v_pk_fma_f32 v[110:111], v[36:37], v[84:85], v[44:45]
	s_nop 0
	v_add_f32_e32 v84, v110, v86
	v_add_f32_e32 v86, v111, v84
	v_pk_mul_f32 v[84:85], v[114:115], v[2:3] op_sel_hi:[1,0]
	v_cvt_pk_bf16_f32 v104, v110, v111
	v_pk_fma_f32 v[88:89], v[38:39], v[84:85], v[46:47]
	s_nop 0
	v_add_f32_e32 v84, v88, v86
	v_add_f32_e32 v108, v89, v84
	v_pk_mul_f32 v[84:85], v[142:143], v[2:3] op_sel_hi:[1,0]
	v_cvt_pk_bf16_f32 v105, v88, v89
	v_pk_fma_f32 v[86:87], v[40:41], v[84:85], v[48:49]
	s_nop 0
	v_add_f32_e32 v84, v86, v108
	v_add_f32_e32 v108, v87, v84
	v_pk_mul_f32 v[84:85], v[106:107], v[2:3] op_sel_hi:[1,0]
	s_nop 0
	v_pk_fma_f32 v[84:85], v[42:43], v[84:85], v[50:51]
	s_nop 0
	v_add_f32_e32 v106, v84, v108
	v_pk_mul_f32 v[108:109], v[116:117], v[2:3] op_sel_hi:[1,0]
	v_add_f32_e32 v114, v85, v106
	v_pk_fma_f32 v[108:109], v[52:53], v[108:109], v[60:61]
	v_cvt_pk_bf16_f32 v106, v86, v87
	v_add_f32_e32 v114, v108, v114
	v_add_f32_e32 v116, v109, v114
	v_pk_mul_f32 v[114:115], v[118:119], v[2:3] op_sel_hi:[1,0]
	v_cvt_pk_bf16_f32 v107, v84, v85
	v_pk_fma_f32 v[132:133], v[54:55], v[114:115], v[62:63]
	v_cvt_pk_bf16_f32 v124, v108, v109
	v_add_f32_e32 v114, v132, v116
	v_add_f32_e32 v116, v133, v114
	v_pk_mul_f32 v[114:115], v[126:127], v[2:3] op_sel_hi:[1,0]
	global_store_dwordx4 v[130:131], v[98:101], off offset:1024
	global_store_dwordx4 v[130:131], v[104:107], off offset:2048
	v_pk_fma_f32 v[126:127], v[56:57], v[114:115], v[64:65]
	v_cvt_pk_bf16_f32 v125, v132, v133
	v_add_f32_e32 v114, v126, v116
	v_add_f32_e32 v116, v127, v114
	v_pk_mul_f32 v[114:115], v[128:129], v[2:3] op_sel_hi:[1,0]
	ds_read_b128 v[104:107], v172 offset:16384
	v_pk_fma_f32 v[128:129], v[58:59], v[114:115], v[66:67]
	s_nop 0
	v_add_f32_e32 v2, v128, v116
	v_add_f32_e32 v2, v129, v2
	s_nop 1
	v_add_f32_dpp v2, v2, v2 quad_perm:[1,0,3,2] row_mask:0xf bank_mask:0xf bound_ctrl:1
	s_nop 1
	v_add_f32_dpp v2, v2, v2 quad_perm:[2,3,0,1] row_mask:0xf bank_mask:0xf bound_ctrl:1
	s_nop 1
	v_add_f32_dpp v2, v2, v2 row_ror:4 row_mask:0xf bank_mask:0xf bound_ctrl:1
	s_nop 1
	v_add_f32_dpp v2, v2, v2 row_ror:8 row_mask:0xf bank_mask:0xf bound_ctrl:1
	s_nop 0
	v_readlane_b32 s6, v2, 16
	v_readlane_b32 s42, v2, 48
	v_readlane_b32 s8, v2, 0
	v_readlane_b32 s9, v2, 32
	v_mov_b32_e32 v114, s6
	v_mov_b32_e32 v115, s42
	v_pk_add_f32 v[114:115], s[8:9], v[114:115]
	s_nop 0
	v_add_f32_e32 v114, v114, v115
	v_fmac_f32_e32 v123, 0xba000000, v114
	v_fmamk_f32 v122, v114, 0xba000000, v122
	v_mul_f32_e32 v116, v123, v123
	v_fmac_f32_e32 v116, v122, v122
	v_fmamk_f32 v120, v114, 0xba000000, v120
	v_fmac_f32_e32 v116, v120, v120
	v_fmac_f32_e32 v121, 0xba000000, v114
	v_fmac_f32_e32 v116, v121, v121
	v_fmamk_f32 v102, v114, 0xba000000, v102
	v_fmac_f32_e32 v116, v102, v102
	v_fmac_f32_e32 v103, 0xba000000, v114
	v_fmac_f32_e32 v116, v103, v103
	v_fmamk_f32 v136, v114, 0xba000000, v96
	v_fmac_f32_e32 v116, v136, v136
	v_fmac_f32_e32 v97, 0xba000000, v114
	v_fmac_f32_e32 v116, v97, v97
	v_fmamk_f32 v112, v114, 0xba000000, v112
	v_fmac_f32_e32 v116, v112, v112
	v_fmac_f32_e32 v113, 0xba000000, v114
	v_fmac_f32_e32 v116, v113, v113
	v_fmamk_f32 v94, v114, 0xba000000, v94
	v_fmac_f32_e32 v116, v94, v94
	v_fmac_f32_e32 v95, 0xba000000, v114
	v_fmac_f32_e32 v116, v95, v95
	v_fmamk_f32 v92, v114, 0xba000000, v92
	v_fmac_f32_e32 v116, v92, v92
	v_fmac_f32_e32 v93, 0xba000000, v114
	v_fmac_f32_e32 v116, v93, v93
	v_fmamk_f32 v90, v114, 0xba000000, v90
	v_fmac_f32_e32 v116, v90, v90
	v_fmac_f32_e32 v91, 0xba000000, v114
	v_fmac_f32_e32 v116, v91, v91
	v_fmamk_f32 v110, v114, 0xba000000, v110
	v_fmac_f32_e32 v116, v110, v110
	v_fmac_f32_e32 v111, 0xba000000, v114
	v_fmac_f32_e32 v116, v111, v111
	v_fmamk_f32 v88, v114, 0xba000000, v88
	v_fmac_f32_e32 v116, v88, v88
	v_fmac_f32_e32 v89, 0xba000000, v114
	v_fmac_f32_e32 v116, v89, v89
	v_fmamk_f32 v86, v114, 0xba000000, v86
	v_fmac_f32_e32 v116, v86, v86
	v_fmac_f32_e32 v87, 0xba000000, v114
	v_fmac_f32_e32 v116, v87, v87
	v_fmamk_f32 v84, v114, 0xba000000, v84
	v_fmac_f32_e32 v116, v84, v84
	v_fmac_f32_e32 v85, 0xba000000, v114
	v_mul_f32_e32 v2, 0x3a000000, v114
	v_fmac_f32_e32 v116, v85, v85
	v_fmamk_f32 v108, v114, 0xba000000, v108
	v_fmac_f32_e32 v116, v108, v108
	v_fmac_f32_e32 v109, 0xba000000, v114
	v_pk_add_f32 v[118:119], v[132:133], v[2:3] op_sel_hi:[1,0] neg_lo:[0,1] neg_hi:[0,1]
	v_fmac_f32_e32 v116, v109, v109
	v_pk_mul_f32 v[114:115], v[118:119], v[118:119]
	s_nop 0
	v_add_f32_e32 v96, v114, v116
	v_pk_add_f32 v[116:117], v[126:127], v[2:3] op_sel_hi:[1,0] neg_lo:[0,1] neg_hi:[0,1]
	v_add_f32_e32 v96, v115, v96
	v_pk_mul_f32 v[114:115], v[116:117], v[116:117]
	v_cvt_pk_bf16_f32 v126, v126, v127
	v_add_f32_e32 v96, v114, v96
	v_add_f32_e32 v96, v115, v96
	v_pk_add_f32 v[114:115], v[128:129], v[2:3] op_sel_hi:[1,0] neg_lo:[0,1] neg_hi:[0,1]
	v_cvt_pk_bf16_f32 v127, v128, v129
	v_pk_mul_f32 v[134:135], v[114:115], v[114:115]
	global_store_dwordx4 v[130:131], v[124:127], off offset:3072
	v_add_f32_e32 v2, v134, v96
	v_add_f32_e32 v2, v135, v2
	ds_read_b128 v[124:127], v172 offset:40960
	ds_read_b128 v[128:131], v172 offset:41984
	v_add_f32_dpp v2, v2, v2 quad_perm:[1,0,3,2] row_mask:0xf bank_mask:0xf bound_ctrl:1
	s_nop 1
	v_add_f32_dpp v2, v2, v2 quad_perm:[2,3,0,1] row_mask:0xf bank_mask:0xf bound_ctrl:1
	s_nop 1
	v_add_f32_dpp v2, v2, v2 row_ror:4 row_mask:0xf bank_mask:0xf bound_ctrl:1
	s_nop 1
	v_add_f32_dpp v2, v2, v2 row_ror:8 row_mask:0xf bank_mask:0xf bound_ctrl:1
	s_nop 0
	v_readlane_b32 s6, v2, 16
	v_readlane_b32 s42, v2, 48
	v_readlane_b32 s8, v2, 0
	v_readlane_b32 s9, v2, 32
	v_mov_b32_e32 v134, s6
	v_mov_b32_e32 v135, s42
	v_pk_add_f32 v[134:135], s[8:9], v[134:135]
	s_mov_b32 s6, 0x3d300000
	v_add_f32_e32 v2, v134, v135
	v_fmamk_f32 v2, v2, 0x3a000000, v207
	v_mul_f32_e32 v96, 0x4f800000, v2
	v_cmp_gt_f32_e32 vcc, s10, v2
	s_nop 1
	v_cndmask_b32_e32 v2, v2, v96, vcc
	v_sqrt_f32_e32 v96, v2
	s_nop 0
	v_add_u32_e32 v98, -1, v96
	v_fma_f32 v99, -v98, v96, v2
	v_cmp_ge_f32_e64 s[42:43], 0, v99
	v_add_u32_e32 v99, 1, v96
	s_nop 0
	v_cndmask_b32_e64 v98, v96, v98, s[42:43]
	v_fma_f32 v96, -v99, v96, v2
	v_cmp_lt_f32_e64 s[42:43], 0, v96
	s_nop 1
	v_cndmask_b32_e64 v96, v98, v99, s[42:43]
	v_mul_f32_e32 v98, 0x37800000, v96
	v_cndmask_b32_e32 v96, v96, v98, vcc
	v_cmp_class_f32_e32 vcc, v2, v208
	s_nop 1
	v_cndmask_b32_e32 v2, v96, v2, vcc
	v_div_scale_f32 v96, s[8:9], v2, v2, 1.0
	v_rcp_f32_e32 v98, v96
	s_nop 0
	v_fma_f32 v99, -v96, v98, 1.0
	v_fmac_f32_e32 v98, v99, v98
	v_div_scale_f32 v99, vcc, 1.0, v2, 1.0
	v_mul_f32_e32 v100, v99, v98
	v_fma_f32 v101, -v96, v100, v99
	v_fmac_f32_e32 v100, v101, v98
	v_fma_f32 v96, -v96, v100, v99
	v_div_fmas_f32 v96, v96, v98, v100
	v_div_fixup_f32 v2, v96, v2, 1.0
	v_mul_f32_e32 v96, v122, v2
	s_waitcnt lgkmcnt(1)
	v_add_f32_e32 v122, 1.0, v124
	ds_read_b128 v[98:101], v172 offset:17408
	v_fma_f32 v132, v122, v96, v104
	v_mul_f32_e32 v96, v123, v2
	v_add_f32_e32 v104, 1.0, v125
	v_fma_f32 v133, v104, v96, v105
	v_mul_f32_e32 v96, v120, v2
	v_add_f32_e32 v104, 1.0, v126
	v_fma_f32 v106, v104, v96, v106
	v_mul_f32_e32 v96, v121, v2
	v_add_f32_e32 v104, 1.0, v127
	v_fmac_f32_e32 v107, v104, v96
	v_max_f32_e64 v104, |v132|, |v133|
	v_max_f32_e64 v105, |v106|, |v107|
	v_max3_f32 v104, v104, 0, v105
	v_mul_f32_e32 v102, v102, v2
	s_waitcnt lgkmcnt(1)
	v_add_f32_e32 v105, 1.0, v128
	s_waitcnt lgkmcnt(0)
	v_fma_f32 v134, v102, v105, v98
	v_mul_f32_e32 v98, v103, v2
	v_add_f32_e32 v102, 1.0, v129
	v_fma_f32 v135, v98, v102, v99
	v_mul_f32_e32 v98, v136, v2
	v_add_f32_e32 v99, 1.0, v130
	v_fma_f32 v100, v98, v99, v100
	v_mul_f32_e32 v97, v97, v2
	v_add_f32_e32 v98, 1.0, v131
	v_mov_b32_e32 v96, v3
	v_fmac_f32_e32 v101, v97, v98
	v_mov_b32_e32 v97, v3
	v_cvt_pk_fp8_f32 v96, v132, v133
	v_cvt_pk_fp8_f32 v97, v134, v135
	v_max_f32_e64 v98, |v134|, |v135|
	v_max_f32_e64 v99, |v100|, |v101|
	ds_read_b128 v[120:123], v172 offset:43008
	ds_read_b128 v[124:127], v172 offset:44032
	v_max3_f32 v130, v104, v98, v99
	ds_read_b128 v[102:105], v172 offset:18432
	v_cvt_pk_fp8_f32 v96, v106, v107 op_sel:[0,0,1]
	v_cvt_pk_fp8_f32 v97, v100, v101 op_sel:[0,0,1]
	v_lshl_add_u64 v[98:99], s[4:5], 0, v[146:147]
	v_add_co_u32_e32 v128, vcc, s6, v98
	v_mul_f32_e32 v112, v112, v2
	s_nop 0
	v_addc_co_u32_e32 v129, vcc, 0, v99, vcc
	s_waitcnt lgkmcnt(2)
	v_add_f32_e32 v120, 1.0, v120
	global_store_dwordx2 v[128:129], v[96:97], off
	ds_read_b128 v[96:99], v172 offset:19456
	s_waitcnt lgkmcnt(1)
	v_fma_f32 v131, v112, v120, v102
	v_mul_f32_e32 v102, v113, v2
	v_add_f32_e32 v112, 1.0, v121
	v_fma_f32 v136, v102, v112, v103
	v_mul_f32_e32 v94, v94, v2
	v_add_f32_e32 v102, 1.0, v122
	v_fma_f32 v104, v94, v102, v104
	v_mul_f32_e32 v94, v95, v2
	v_add_f32_e32 v95, 1.0, v123
	v_fmac_f32_e32 v105, v94, v95
	v_max_f32_e64 v94, |v131|, |v136|
	v_max_f32_e64 v95, |v104|, |v105|
	v_max3_f32 v94, v130, v94, v95
	v_mul_f32_e32 v92, v92, v2
	v_add_f32_e32 v95, 1.0, v124
	s_waitcnt lgkmcnt(0)
	v_fma_f32 v130, v92, v95, v96
	v_mul_f32_e32 v92, v93, v2
	v_add_f32_e32 v93, 1.0, v125
	v_fma_f32 v137, v92, v93, v97
	v_mul_f32_e32 v90, v90, v2
	v_add_f32_e32 v92, 1.0, v126
	v_fma_f32 v98, v90, v92, v98
	v_mul_f32_e32 v90, v91, v2
	v_add_f32_e32 v91, 1.0, v127
	v_fmac_f32_e32 v99, v90, v91
	v_max_f32_e64 v90, |v130|, |v137|
	v_max_f32_e64 v91, |v98|, |v99|
	ds_read_b128 v[120:123], v172 offset:45056
	ds_read_b128 v[124:127], v172 offset:46080
	v_max3_f32 v112, v94, v90, v91
	ds_read_b128 v[94:97], v172 offset:20480
	ds_read_b128 v[90:93], v172 offset:21504
	v_mul_f32_e32 v110, v110, v2
	s_waitcnt lgkmcnt(3)
	v_add_f32_e32 v113, 1.0, v120
	v_mul_f32_e32 v88, v88, v2
	s_waitcnt lgkmcnt(1)
	v_fma_f32 v138, v110, v113, v94
	v_mul_f32_e32 v94, v111, v2
	v_add_f32_e32 v110, 1.0, v121
	v_fma_f32 v139, v94, v110, v95
	v_add_f32_e32 v94, 1.0, v122
	v_fma_f32 v96, v88, v94, v96
	v_mul_f32_e32 v88, v89, v2
	v_add_f32_e32 v89, 1.0, v123
	v_fmac_f32_e32 v97, v88, v89
	v_max_f32_e64 v88, |v138|, |v139|
	v_max_f32_e64 v89, |v96|, |v97|
	v_max3_f32 v88, v112, v88, v89
	v_mul_f32_e32 v86, v86, v2
	v_add_f32_e32 v89, 1.0, v124
	s_waitcnt lgkmcnt(0)
	v_fma_f32 v124, v86, v89, v90
	v_mul_f32_e32 v86, v87, v2
	v_add_f32_e32 v87, 1.0, v125
	v_fma_f32 v125, v86, v87, v91
	v_mul_f32_e32 v84, v84, v2
	v_add_f32_e32 v86, 1.0, v126
	v_fma_f32 v92, v84, v86, v92
	v_mul_f32_e32 v84, v85, v2
	v_add_f32_e32 v85, 1.0, v127
	v_fmac_f32_e32 v93, v84, v85
	v_max_f32_e64 v84, |v124|, |v125|
	v_max_f32_e64 v85, |v92|, |v93|
	ds_read_b128 v[110:113], v172 offset:47104
	ds_read_b128 v[120:123], v172 offset:48128
	v_max3_f32 v126, v88, v84, v85
	ds_read_b128 v[88:91], v172 offset:22528
	ds_read_b128 v[84:87], v172 offset:23552
	v_mul_f32_e32 v108, v108, v2
	s_waitcnt lgkmcnt(3)
	v_add_f32_e32 v110, 1.0, v110
	v_mov_b32_e32 v102, v3
	s_waitcnt lgkmcnt(1)
	v_fma_f32 v108, v108, v110, v88
	v_mul_f32_e32 v88, v109, v2
	v_add_f32_e32 v109, 1.0, v111
	v_fma_f32 v109, v88, v109, v89
	v_mul_f32_e32 v88, v118, v2
	v_add_f32_e32 v89, 1.0, v112
	v_fma_f32 v90, v88, v89, v90
	v_mul_f32_e32 v88, v119, v2
	v_add_f32_e32 v89, 1.0, v113
	v_fmac_f32_e32 v91, v88, v89
	v_max_f32_e64 v89, |v108|, |v109|
	v_max_f32_e64 v110, |v90|, |v91|
	v_max3_f32 v110, v126, v89, v110
	v_mul_f32_e32 v89, v116, v2
	v_add_f32_e32 v111, 1.0, v120
	s_waitcnt lgkmcnt(0)
	v_fma_f32 v111, v89, v111, v84
	v_mul_f32_e32 v84, v117, v2
	v_add_f32_e32 v89, 1.0, v121
	v_fma_f32 v112, v84, v89, v85
	v_mul_f32_e32 v84, v114, v2
	v_add_f32_e32 v85, 1.0, v122
	v_fma_f32 v86, v84, v85, v86
	v_mul_f32_e32 v2, v115, v2
	v_add_f32_e32 v84, 1.0, v123
	v_fmac_f32_e32 v87, v2, v84
	v_max_f32_e64 v2, |v111|, |v112|
	v_max_f32_e64 v84, |v86|, |v87|
	v_max3_f32 v2, v110, v2, v84
	v_mov_b32_e32 v103, v3
	v_cvt_pk_fp8_f32 v102, v131, v136
	v_mov_b32_dpp v84, v2 quad_perm:[1,0,3,2] row_mask:0xf bank_mask:0xf bound_ctrl:1
	v_max_f32_e32 v84, v84, v84
	v_max_f32_e32 v2, v2, v84
	v_cvt_pk_fp8_f32 v103, v130, v137
	v_mov_b32_e32 v94, v3
	v_mov_b32_dpp v84, v2 quad_perm:[2,3,0,1] row_mask:0xf bank_mask:0xf bound_ctrl:1
	v_max_f32_e32 v84, v84, v84
	v_max_f32_e32 v2, v2, v84
	v_mov_b32_e32 v95, v3
	v_cvt_pk_fp8_f32 v94, v138, v139
	v_mov_b32_dpp v84, v2 row_ror:4 row_mask:0xf bank_mask:0xf bound_ctrl:1
	v_max_f32_e32 v84, v84, v84
	v_max_f32_e32 v2, v2, v84
	v_cvt_pk_fp8_f32 v95, v124, v125
	v_mov_b32_e32 v88, v3
	v_mov_b32_dpp v84, v2 row_ror:8 row_mask:0xf bank_mask:0xf bound_ctrl:1
	v_max_f32_e32 v84, v84, v84
	v_max_f32_e32 v2, v2, v84
	v_mov_b32_e32 v89, v3
	v_readlane_b32 s9, v2, 32
	v_readlane_b32 s42, v2, 48
	v_readlane_b32 s6, v2, 0
	v_readlane_b32 s8, v2, 16
	v_max_f32_e64 v2, s42, s42
	v_max_f32_e64 v84, s9, s9
	v_max_f32_e32 v2, v84, v2
	v_mov_b32_e32 v84, s8
	v_cvt_pk_fp8_f32 v88, v108, v109
	v_cvt_pk_fp8_f32 v89, v111, v112
	v_max3_f32 v2, s6, v84, v2
	v_div_scale_f32 v84, s[8:9], v2, v2, s79
	v_cvt_pk_fp8_f32 v102, v104, v105 op_sel:[0,0,1]
	v_cvt_pk_fp8_f32 v103, v98, v99 op_sel:[0,0,1]
	v_rcp_f32_e32 v85, v84
	v_cvt_pk_fp8_f32 v94, v96, v97 op_sel:[0,0,1]
	v_cvt_pk_fp8_f32 v95, v92, v93 op_sel:[0,0,1]
	v_cvt_pk_fp8_f32 v88, v90, v91 op_sel:[0,0,1]
	v_cvt_pk_fp8_f32 v89, v86, v87 op_sel:[0,0,1]
	global_store_dwordx2 v[128:129], v[102:103], off offset:512
	global_store_dwordx2 v[128:129], v[94:95], off offset:1024
	global_store_dwordx2 v[128:129], v[88:89], off offset:1536
	v_fma_f32 v88, -v84, v85, 1.0
	v_fmac_f32_e32 v85, v88, v85
	v_div_scale_f32 v88, vcc, s79, v2, s79
	v_mul_f32_e32 v89, v88, v85
	v_fma_f32 v94, -v84, v89, v88
	v_fmac_f32_e32 v89, v94, v85
	v_fma_f32 v84, -v84, v89, v88
	v_div_fmas_f32 v84, v84, v85, v89
	v_div_fixup_f32 v84, v84, v2, s79
	v_cmp_lt_f32_e32 vcc, 0, v2
	s_mov_b32 s6, 0x13400000
	s_nop 0
	v_cndmask_b32_e32 v88, 1.0, v84, vcc
	v_mul_f32_e32 v89, v132, v88
	v_mul_f32_e32 v94, v133, v88
	v_rndne_f32_e32 v89, v89
	v_rndne_f32_e32 v94, v94
	v_cvt_i32_f32_e32 v89, v89
	v_cvt_i32_f32_e32 v94, v94
	v_mul_f32_e32 v103, v106, v88
	v_mul_f32_e32 v106, v107, v88
	v_rndne_f32_e32 v103, v103
	v_rndne_f32_e32 v106, v106
	v_cvt_i32_f32_e32 v103, v103
	v_cvt_i32_f32_e32 v106, v106
	v_bfe_i32 v95, v89, 0, 4
	v_bfe_i32 v102, v94, 0, 4
	v_sub_u32_e32 v95, v89, v95
	v_sub_u32_e32 v102, v94, v102
	v_mul_f32_e32 v110, v134, v88
	v_lshrrev_b32_e32 v95, 4, v95
	v_and_b32_e32 v102, 0xf0, v102
	v_rndne_f32_e32 v110, v110
	v_and_or_b32 v95, v95, 15, v102
	v_bfe_i32 v102, v103, 0, 4
	v_bfe_i32 v107, v106, 0, 4
	v_cvt_i32_f32_e32 v110, v110
	v_sub_u32_e32 v102, v103, v102
	v_sub_u32_e32 v107, v106, v107
	v_lshlrev_b32_e32 v102, 4, v102
	v_lshlrev_b32_e32 v107, 8, v107
	v_and_b32_e32 v102, 0xf00, v102
	v_and_b32_e32 v107, 0xf000, v107
	v_or3_b32 v95, v95, v102, v107
	v_bfe_i32 v102, v110, 0, 4
	v_sub_u32_e32 v102, v110, v102
	v_lshlrev_b32_e32 v107, 16, v110
	v_mul_f32_e32 v110, v135, v88
	v_rndne_f32_e32 v110, v110
	v_cvt_i32_f32_e32 v110, v110
	v_mul_f32_e32 v100, v100, v88
	v_rndne_f32_e32 v100, v100
	v_mul_f32_e32 v101, v101, v88
	v_cvt_i32_f32_e32 v100, v100
	v_rndne_f32_e32 v101, v101
	v_bfe_i32 v113, v110, 0, 4
	v_cvt_i32_f32_e32 v101, v101
	v_lshlrev_b32_e32 v102, 12, v102
	v_sub_u32_sdwa v113, v110, v113 dst_sel:WORD_1 dst_unused:UNUSED_PAD src0_sel:DWORD src1_sel:DWORD
	v_lshlrev_b32_e32 v94, 4, v94
	v_and_b32_e32 v102, 0xf0000, v102
	v_and_b32_e32 v113, 0xf00000, v113
	v_and_b32_e32 v94, 0xf0, v94
	v_lshlrev_b32_e32 v103, 8, v103
	v_lshlrev_b32_e32 v106, 12, v106
	v_or3_b32 v95, v95, v102, v113
	v_bfe_i32 v102, v100, 0, 4
	v_and_b32_e32 v103, 0xf00, v103
	v_and_b32_e32 v106, 0xf000, v106
	v_lshlrev_b32_e32 v110, 20, v110
	v_sub_u32_e32 v102, v100, v102
	v_bfe_i32 v114, v101, 0, 4
	v_and_or_b32 v89, v89, 15, v94
	v_lshl_add_u64 v[84:85], s[4:5], 0, v[148:149]
	v_and_b32_e32 v107, 0xf0000, v107
	v_and_b32_e32 v110, 0xf00000, v110
	v_lshlrev_b32_e32 v100, 24, v100
	v_lshlrev_b32_e32 v102, 20, v102
	v_lshlrev_b32_e32 v113, 28, v101
	v_sub_u32_sdwa v101, v101, v114 dst_sel:BYTE_3 dst_unused:UNUSED_PAD src0_sel:DWORD src1_sel:DWORD
	v_or3_b32 v89, v89, v103, v106
	v_and_b32_e32 v100, 0xf000000, v100
	v_and_b32_e32 v102, 0xf000000, v102
	v_or3_b32 v89, v89, v107, v110
	v_and_b32_e32 v94, 0xf0000000, v101
	v_add_co_u32_e64 v84, s[42:43], s6, v84
	v_or3_b32 v89, v89, v100, v113
	v_or3_b32 v94, v95, v102, v94
	v_addc_co_u32_e64 v85, s[42:43], 0, v85, s[42:43]
	global_store_dword v[84:85], v94, off
	global_store_dword v[84:85], v89, off offset:1024
	v_mul_f32_e32 v89, v131, v88
	v_mul_f32_e32 v94, v136, v88
	v_rndne_f32_e32 v89, v89
	v_rndne_f32_e32 v94, v94
	v_cvt_i32_f32_e32 v89, v89
	v_cvt_i32_f32_e32 v94, v94
	v_mul_f32_e32 v101, v104, v88
	v_mul_f32_e32 v102, v105, v88
	v_rndne_f32_e32 v101, v101
	v_rndne_f32_e32 v102, v102
	v_cvt_i32_f32_e32 v101, v101
	v_cvt_i32_f32_e32 v102, v102
	v_bfe_i32 v95, v89, 0, 4
	v_bfe_i32 v100, v94, 0, 4
	v_sub_u32_e32 v95, v89, v95
	v_sub_u32_e32 v100, v94, v100
	v_mul_f32_e32 v104, v130, v88
	v_lshrrev_b32_e32 v95, 4, v95
	v_and_b32_e32 v100, 0xf0, v100
	v_rndne_f32_e32 v104, v104
	v_and_or_b32 v95, v95, 15, v100
	v_bfe_i32 v100, v101, 0, 4
	v_bfe_i32 v103, v102, 0, 4
	v_cvt_i32_f32_e32 v104, v104
	v_sub_u32_e32 v100, v101, v100
	v_sub_u32_e32 v103, v102, v103
	v_lshlrev_b32_e32 v100, 4, v100
	v_lshlrev_b32_e32 v103, 8, v103
	v_and_b32_e32 v100, 0xf00, v100
	v_and_b32_e32 v103, 0xf000, v103
	v_or3_b32 v95, v95, v100, v103
	v_bfe_i32 v100, v104, 0, 4
	v_sub_u32_e32 v100, v104, v100
	v_lshlrev_b32_e32 v103, 16, v104
	v_mul_f32_e32 v104, v137, v88
	v_rndne_f32_e32 v104, v104
	v_cvt_i32_f32_e32 v104, v104
	v_mul_f32_e32 v98, v98, v88
	v_rndne_f32_e32 v98, v98
	v_mul_f32_e32 v99, v99, v88
	v_cvt_i32_f32_e32 v98, v98
	v_rndne_f32_e32 v99, v99
	v_bfe_i32 v105, v104, 0, 4
	v_cvt_i32_f32_e32 v99, v99
	v_lshlrev_b32_e32 v100, 12, v100
	v_sub_u32_sdwa v105, v104, v105 dst_sel:WORD_1 dst_unused:UNUSED_PAD src0_sel:DWORD src1_sel:DWORD
	v_lshlrev_b32_e32 v94, 4, v94
	v_and_b32_e32 v100, 0xf0000, v100
	v_and_b32_e32 v105, 0xf00000, v105
	v_and_b32_e32 v94, 0xf0, v94
	v_lshlrev_b32_e32 v101, 8, v101
	v_lshlrev_b32_e32 v102, 12, v102
	v_or3_b32 v95, v95, v100, v105
	v_bfe_i32 v100, v98, 0, 4
	v_and_b32_e32 v101, 0xf00, v101
	v_and_b32_e32 v102, 0xf000, v102
	v_lshlrev_b32_e32 v104, 20, v104
	v_sub_u32_e32 v100, v98, v100
	v_bfe_i32 v106, v99, 0, 4
	v_and_or_b32 v89, v89, 15, v94
	v_and_b32_e32 v103, 0xf0000, v103
	v_and_b32_e32 v104, 0xf00000, v104
	v_lshlrev_b32_e32 v98, 24, v98
	v_lshlrev_b32_e32 v100, 20, v100
	v_lshlrev_b32_e32 v105, 28, v99
	v_sub_u32_sdwa v99, v99, v106 dst_sel:BYTE_3 dst_unused:UNUSED_PAD src0_sel:DWORD src1_sel:DWORD
	v_or3_b32 v89, v89, v101, v102
	v_and_b32_e32 v98, 0xf000000, v98
	v_and_b32_e32 v100, 0xf000000, v100
	v_or3_b32 v89, v89, v103, v104
	v_and_b32_e32 v94, 0xf0000000, v99
	v_or3_b32 v89, v89, v98, v105
	v_or3_b32 v94, v95, v100, v94
	global_store_dword v[84:85], v94, off offset:256
	global_store_dword v[84:85], v89, off offset:1280
	v_mul_f32_e32 v89, v138, v88
	v_mul_f32_e32 v94, v139, v88
	v_rndne_f32_e32 v89, v89
	v_rndne_f32_e32 v94, v94
	v_cvt_i32_f32_e32 v89, v89
	v_cvt_i32_f32_e32 v94, v94
	v_mul_f32_e32 v96, v96, v88
	v_mul_f32_e32 v97, v97, v88
	v_rndne_f32_e32 v96, v96
	v_rndne_f32_e32 v97, v97
	v_cvt_i32_f32_e32 v96, v96
	v_cvt_i32_f32_e32 v97, v97
	v_bfe_i32 v95, v89, 0, 4
	v_bfe_i32 v98, v94, 0, 4
	v_sub_u32_e32 v95, v89, v95
	v_sub_u32_e32 v98, v94, v98
	v_mul_f32_e32 v100, v124, v88
	v_lshrrev_b32_e32 v95, 4, v95
	v_and_b32_e32 v98, 0xf0, v98
	v_rndne_f32_e32 v100, v100
	v_and_or_b32 v95, v95, 15, v98
	v_bfe_i32 v98, v96, 0, 4
	v_bfe_i32 v99, v97, 0, 4
	v_cvt_i32_f32_e32 v100, v100
	v_sub_u32_e32 v98, v96, v98
	v_sub_u32_e32 v99, v97, v99
	v_lshlrev_b32_e32 v98, 4, v98
	v_lshlrev_b32_e32 v99, 8, v99
	v_and_b32_e32 v98, 0xf00, v98
	v_and_b32_e32 v99, 0xf000, v99
	v_or3_b32 v95, v95, v98, v99
	v_bfe_i32 v98, v100, 0, 4
	v_sub_u32_e32 v98, v100, v98
	v_lshlrev_b32_e32 v99, 16, v100
	v_mul_f32_e32 v100, v125, v88
	v_rndne_f32_e32 v100, v100
	v_cvt_i32_f32_e32 v100, v100
	v_mul_f32_e32 v92, v92, v88
	v_rndne_f32_e32 v92, v92
	v_mul_f32_e32 v93, v93, v88
	v_cvt_i32_f32_e32 v92, v92
	v_rndne_f32_e32 v93, v93
	v_bfe_i32 v101, v100, 0, 4
	v_cvt_i32_f32_e32 v93, v93
	v_lshlrev_b32_e32 v94, 4, v94
	v_lshlrev_b32_e32 v98, 12, v98
	v_sub_u32_sdwa v101, v100, v101 dst_sel:WORD_1 dst_unused:UNUSED_PAD src0_sel:DWORD src1_sel:DWORD
	v_and_b32_e32 v94, 0xf0, v94
	v_lshlrev_b32_e32 v96, 8, v96
	v_lshlrev_b32_e32 v97, 12, v97
	v_and_b32_e32 v98, 0xf0000, v98
	v_and_b32_e32 v101, 0xf00000, v101
	v_and_b32_e32 v96, 0xf00, v96
	v_and_b32_e32 v97, 0xf000, v97
	v_lshlrev_b32_e32 v100, 20, v100
	v_or3_b32 v95, v95, v98, v101
	v_bfe_i32 v98, v92, 0, 4
	v_and_or_b32 v89, v89, 15, v94
	v_and_b32_e32 v99, 0xf0000, v99
	v_and_b32_e32 v100, 0xf00000, v100
	v_sub_u32_e32 v98, v92, v98
	v_lshlrev_b32_e32 v92, 24, v92
	v_bfe_i32 v102, v93, 0, 4
	v_or3_b32 v89, v89, v96, v97
	v_and_b32_e32 v92, 0xf000000, v92
	v_lshlrev_b32_e32 v98, 20, v98
	v_lshlrev_b32_e32 v101, 28, v93
	v_sub_u32_sdwa v93, v93, v102 dst_sel:BYTE_3 dst_unused:UNUSED_PAD src0_sel:DWORD src1_sel:DWORD
	v_or3_b32 v89, v89, v99, v100
	v_and_b32_e32 v98, 0xf000000, v98
	v_or3_b32 v89, v89, v92, v101
	v_and_b32_e32 v92, 0xf0000000, v93
	v_or3_b32 v92, v95, v98, v92
	global_store_dword v[84:85], v92, off offset:512
	global_store_dword v[84:85], v89, off offset:1536
	v_mul_f32_e32 v89, v108, v88
	v_mul_f32_e32 v92, v109, v88
	v_rndne_f32_e32 v89, v89
	v_rndne_f32_e32 v92, v92
	v_cvt_i32_f32_e32 v89, v89
	v_cvt_i32_f32_e32 v92, v92
	v_mul_f32_e32 v90, v90, v88
	v_mul_f32_e32 v91, v91, v88
	v_rndne_f32_e32 v90, v90
	v_rndne_f32_e32 v91, v91
	v_cvt_i32_f32_e32 v90, v90
	v_cvt_i32_f32_e32 v91, v91
	v_bfe_i32 v93, v89, 0, 4
	v_bfe_i32 v94, v92, 0, 4
	v_sub_u32_e32 v93, v89, v93
	v_sub_u32_e32 v94, v92, v94
	v_mul_f32_e32 v96, v111, v88
	v_lshrrev_b32_e32 v93, 4, v93
	v_and_b32_e32 v94, 0xf0, v94
	v_rndne_f32_e32 v96, v96
	v_and_or_b32 v93, v93, 15, v94
	v_bfe_i32 v94, v90, 0, 4
	v_bfe_i32 v95, v91, 0, 4
	v_cvt_i32_f32_e32 v96, v96
	v_sub_u32_e32 v94, v90, v94
	v_sub_u32_e32 v95, v91, v95
	v_lshlrev_b32_e32 v94, 4, v94
	v_lshlrev_b32_e32 v95, 8, v95
	v_and_b32_e32 v94, 0xf00, v94
	v_and_b32_e32 v95, 0xf000, v95
	v_or3_b32 v93, v93, v94, v95
	v_bfe_i32 v94, v96, 0, 4
	v_sub_u32_e32 v94, v96, v94
	v_lshlrev_b32_e32 v95, 16, v96
	v_mul_f32_e32 v96, v112, v88
	v_rndne_f32_e32 v96, v96
	v_cvt_i32_f32_e32 v96, v96
	v_mul_f32_e32 v86, v86, v88
	v_rndne_f32_e32 v86, v86
	v_mul_f32_e32 v87, v87, v88
	v_cvt_i32_f32_e32 v86, v86
	v_rndne_f32_e32 v87, v87
	v_bfe_i32 v97, v96, 0, 4
	v_cvt_i32_f32_e32 v87, v87
	v_lshlrev_b32_e32 v94, 12, v94
	v_sub_u32_sdwa v97, v96, v97 dst_sel:WORD_1 dst_unused:UNUSED_PAD src0_sel:DWORD src1_sel:DWORD
	v_and_b32_e32 v94, 0xf0000, v94
	v_and_b32_e32 v97, 0xf00000, v97
	v_lshlrev_b32_e32 v92, 4, v92
	v_or3_b32 v93, v93, v94, v97
	v_bfe_i32 v94, v86, 0, 4
	v_and_b32_e32 v92, 0xf0, v92
	v_lshlrev_b32_e32 v90, 8, v90
	v_lshlrev_b32_e32 v91, 12, v91
	v_sub_u32_e32 v94, v86, v94
	v_bfe_i32 v97, v87, 0, 4
	v_and_b32_e32 v90, 0xf00, v90
	v_and_b32_e32 v91, 0xf000, v91
	v_lshlrev_b32_e32 v96, 20, v96
	v_lshlrev_b32_e32 v88, 20, v94
	v_lshlrev_b32_e32 v94, 28, v87
	v_sub_u32_sdwa v87, v87, v97 dst_sel:BYTE_3 dst_unused:UNUSED_PAD src0_sel:DWORD src1_sel:DWORD
	v_and_or_b32 v89, v89, 15, v92
	v_and_b32_e32 v95, 0xf0000, v95
	v_and_b32_e32 v96, 0xf00000, v96
	v_lshlrev_b32_e32 v86, 24, v86
	v_and_b32_e32 v88, 0xf000000, v88
	v_or3_b32 v89, v89, v90, v91
	v_and_b32_e32 v87, 0xf0000000, v87
	v_and_b32_e32 v86, 0xf000000, v86
	v_or3_b32 v89, v89, v95, v96
	v_or3_b32 v87, v93, v88, v87
	v_or3_b32 v86, v89, v86, v94
	global_store_dword v[84:85], v87, off offset:768
	global_store_dword v[84:85], v86, off offset:1792
	s_and_saveexec_b64 s[8:9], s[40:41]
	s_cbranch_execz .LBB0_516
	s_add_u32 s42, s4, s56
	v_mul_f32_e32 v2, 0x3c09ae41, v2
	s_addc_u32 s43, s5, s57
	v_cndmask_b32_e32 v2, 1.0, v2, vcc
	global_store_dword v3, v2, s[42:43]
	s_branch .LBB0_516

	.amdhsa_kernel _Z8skel_fwd4Args
		.amdhsa_group_segment_fixed_size 0
		.amdhsa_private_segment_fixed_size 0
		.amdhsa_kernarg_size 448
		.amdhsa_user_sgpr_count 2
		.amdhsa_user_sgpr_dispatch_ptr 0
		.amdhsa_user_sgpr_queue_ptr 0
		.amdhsa_user_sgpr_kernarg_segment_ptr 1
		.amdhsa_user_sgpr_dispatch_id 0
		.amdhsa_user_sgpr_kernarg_preload_length 0
		.amdhsa_user_sgpr_kernarg_preload_offset 0
		.amdhsa_user_sgpr_private_segment_size 0
		.amdhsa_uses_dynamic_stack 0
		.amdhsa_enable_private_segment 0
		.amdhsa_system_sgpr_workgroup_id_x 1
		.amdhsa_system_sgpr_workgroup_id_y 0
		.amdhsa_system_sgpr_workgroup_id_z 0
		.amdhsa_system_sgpr_workgroup_info 0
		.amdhsa_system_vgpr_workitem_id 0
		.amdhsa_next_free_vgpr 255
		.amdhsa_next_free_sgpr 102
		.amdhsa_accum_offset 256
		.amdhsa_reserve_vcc 1
		.amdhsa_float_round_mode_32 0
		.amdhsa_float_round_mode_16_64 0
		.amdhsa_float_denorm_mode_32 3
		.amdhsa_float_denorm_mode_16_64 3
		.amdhsa_dx10_clamp 1
		.amdhsa_ieee_mode 1
		.amdhsa_fp16_overflow 0
		.amdhsa_tg_split 0
		.amdhsa_exception_fp_ieee_invalid_op 0
		.amdhsa_exception_fp_denorm_src 0
		.amdhsa_exception_fp_ieee_div_zero 0
		.amdhsa_exception_fp_ieee_overflow 0
		.amdhsa_exception_fp_ieee_underflow 0
		.amdhsa_exception_fp_ieee_inexact 0
		.amdhsa_exception_int_div_zero 0
	.end_amdhsa_kernel

amdhsa.kernels:
  - .agpr_count:     0
    .args:
      - .offset:         0
        .size:           192
        .value_kind:     by_value
      - .offset:         192
        .size:           4
        .value_kind:     hidden_block_count_x
      - .offset:         196
        .size:           4
        .value_kind:     hidden_block_count_y
      - .offset:         200
        .size:           4
        .value_kind:     hidden_block_count_z
      - .offset:         204
        .size:           2
        .value_kind:     hidden_group_size_x
      - .offset:         206
        .size:           2
        .value_kind:     hidden_group_size_y
      - .offset:         208
        .size:           2
        .value_kind:     hidden_group_size_z
      - .offset:         210
        .size:           2
        .value_kind:     hidden_remainder_x
      - .offset:         212
        .size:           2
        .value_kind:     hidden_remainder_y
      - .offset:         214
        .size:           2
        .value_kind:     hidden_remainder_z
      - .offset:         232
        .size:           8
        .value_kind:     hidden_global_offset_x
      - .offset:         240
        .size:           8
        .value_kind:     hidden_global_offset_y
      - .offset:         248
        .size:           8
        .value_kind:     hidden_global_offset_z
      - .offset:         256
        .size:           2
        .value_kind:     hidden_grid_dims
      - .offset:         312
        .size:           4
        .value_kind:     hidden_dynamic_lds_size
    .group_segment_fixed_size: 0
    .kernarg_segment_align: 8
    .kernarg_segment_size: 448
    .language:       OpenCL C
    .language_version:
      - 2
      - 0
    .max_flat_workgroup_size: 512
    .name:           _Z8skel_fwd4Args
    .private_segment_fixed_size: 0
    .sgpr_count:     108
    .sgpr_spill_count: 103
    .symbol:         _Z8skel_fwd4Args.kd
    .uniform_work_group_size: 1
    .uses_dynamic_stack: false
    .vgpr_count:     255
    .vgpr_spill_count: 0
    .wavefront_size: 64
